# attention: K/V LDS-DMA issue block moved from step top to behind the second QK MFMA (5 of 6 loop steps)
# speedup vs baseline: 1.0085x; 1.0085x over previous
; __device__ __forceinline__ void finishSM(f32x16& p0, f32x16& p1, float alpha, float& l_reg, v8i& pa) {
; #pragma unroll
;   for (int r = 0; r < 16; ++r) p1[r] = __builtin_amdgcn_exp2f(p1[r]);
;   float ps = 0;
; #pragma unroll
;   for (int r = 0; r < 16; ++r) ps += p0[r];
; #pragma unroll
;   for (int r = 0; r < 16; ++r) ps += p1[r];
;   { auto rr = __builtin_amdgcn_permlane32_swap(__float_as_uint(ps), __float_as_uint(ps), false, false);
;     ps = __uint_as_float(rr[0]) + __uint_as_float(rr[1]); }
;   l_reg = l_reg * alpha + ps;
; #pragma unroll
;   for (int q = 0; q < 4; ++q) { int w0 = pa[q], w1 = pa[4 + q];
;     w0 = __builtin_amdgcn_cvt_pk_fp8_f32(p0[4 * q], p0[4 * q + 1], w0, false); w0 = __builtin_amdgcn_cvt_pk_fp8_f32(p0[4 * q + 2], p0[4 * q + 3], w0, true);
;     w1 = __builtin_amdgcn_cvt_pk_fp8_f32(p1[4 * q], p1[4 * q + 1], w1, false); w1 = __builtin_amdgcn_cvt_pk_fp8_f32(p1[4 * q + 2], p1[4 * q + 3], w1, true);
;     pa[q] = w0; pa[4 + q] = w1; }
; }
; __device__ __forceinline__ void qkt(f32x16& p0, f32x16& p1, const char* Ks, const v8i* qr, int r32, int hi, const f32x16& nm16) {
; #pragma unroll
;   for (int s = 0; s < 3; ++s) { const int c0 = 4 * s + 2 * hi;
;     const v8i a0 = __builtin_shufflevector(*reinterpret_cast<const v4i*>(Ks + k8_off(r32, c0)), *reinterpret_cast<const v4i*>(Ks + k8_off(r32, c0 + 1)), 0, 1, 2, 3, 4, 5, 6, 7);
;     const v8i a1 = __builtin_shufflevector(*reinterpret_cast<const v4i*>(Ks + 32 * DQK + k8_off(r32, c0)), *reinterpret_cast<const v4i*>(Ks + 32 * DQK + k8_off(r32, c0 + 1)), 0, 1, 2, 3, 4, 5, 6, 7);
;     p0 = __builtin_amdgcn_mfma_scale_f32_32x32x64_f8f6f4(a0, qr[s], s == 0 ? nm16 : p0, 0, 0, 0, 0, 0, 0);
;     p1 = __builtin_amdgcn_mfma_scale_f32_32x32x64_f8f6f4(a1, qr[s], s == 0 ? nm16 : p1, 0, 0, 0, 0, 0, 0); }
; }
; __device__ __forceinline__ void pv_d0(f32x16* o, const char* Vs, v8i pa, int r32, int hi) {
; #pragma unroll
;   for (int d0 = 0; d0 < 4; ++d0) { const int row = 32 * d0 + r32, x = (row >> 2) & 3;
;     const v8i vb = __builtin_shufflevector(*reinterpret_cast<const v4i*>(Vs + row * 64 + (((2 * hi) ^ x) << 4)), *reinterpret_cast<const v4i*>(Vs + row * 64 + (((2 * hi + 1) ^ x) << 4)), 0, 1, 2, 3, 4, 5, 6, 7);
;     o[d0] = __builtin_amdgcn_mfma_scale_f32_32x32x64_f8f6f4(pa, vb, o[d0], 0, 0, 0, 0, 0, 0); }
; }
.LBB0_887:
	ds_read_b128 v[98:101], v196 offset:20480
	ds_read_b128 v[102:105], v197 offset:20480
	ds_read_b128 v[206:209], v196 offset:26624
	ds_read_b128 v[210:213], v197 offset:26624
	v_add_f32_e32 v182, 0, v235
	v_add_f32_e32 v182, v236, v182
	s_waitcnt lgkmcnt(0)
	v_mfma_f32_32x32x64_f8f6f4 v[114:129], v[98:105], v[138:145], v[66:81]
	v_add_f32_e32 v182, v233, v182
	v_add_f32_e32 v182, v234, v182
	v_add_f32_e32 v182, v231, v182
	v_add_f32_e32 v182, v232, v182
	v_add_f32_e32 v182, v229, v182
	v_add_f32_e32 v182, v230, v182
	v_add_f32_e32 v182, v227, v182
	v_add_f32_e32 v182, v228, v182
	v_add_f32_e32 v182, v225, v182
	v_add_f32_e32 v182, v226, v182
	v_exp_f32_e32 v82, v82
	v_add_f32_e32 v182, v223, v182
	v_exp_f32_e32 v83, v83
	v_add_f32_e32 v182, v224, v182
	v_exp_f32_e32 v84, v84
	v_mfma_f32_32x32x64_f8f6f4 v[98:113], v[206:213], v[138:145], v[66:81]
	v_lshl_add_u64 v[178:179], s[6:7], 0, v[174:175]
	s_mov_b32 m0, s90
	v_lshl_add_u64 v[238:239], v[178:179], 0, s[24:25]
	global_load_lds_dwordx4 v[238:239], off
	v_cndmask_b32_e64 v238, 0, 1, s[64:65]
	v_cmp_ne_u32_e64 s[4:5], 1, v238
	s_andn2_b64 vcc, exec, s[64:65]
	v_lshl_add_u64 v[180:181], s[6:7], 0, v[172:173]
	s_cbranch_vccnz .LBB0_889
	v_lshl_add_u64 v[238:239], v[180:181], 0, s[24:25]
	s_mov_b32 m0, s91
	s_nop 0
	global_load_lds_dwordx4 v[238:239], off
.LBB0_889:
	v_lshl_add_u64 v[176:177], s[6:7], 0, v[170:171]
	v_lshl_add_u64 v[238:239], v[176:177], 0, s[26:27]
	s_mov_b32 m0, s89
	s_nop 0
	global_load_lds_dwordx4 v[238:239], off
	ds_read_b128 v[206:209], v198 offset:20480
	ds_read_b128 v[210:213], v199 offset:20480
	ds_read_b128 v[238:241], v198 offset:26624
	ds_read_b128 v[242:245], v199 offset:26624
	v_add_f32_e32 v182, v221, v182
	v_exp_f32_e32 v85, v85
	v_add_f32_e32 v182, v222, v182
	v_exp_f32_e32 v86, v86
	v_add_f32_e32 v182, v82, v182
	v_exp_f32_e32 v87, v87
	v_add_f32_e32 v182, v83, v182
	v_exp_f32_e32 v88, v88
	v_add_f32_e32 v182, v84, v182
	v_exp_f32_e32 v89, v89
	v_add_f32_e32 v182, v85, v182
	v_exp_f32_e32 v90, v90
	v_add_f32_e32 v182, v86, v182
	v_exp_f32_e32 v91, v91
	s_waitcnt lgkmcnt(0)
	v_mfma_f32_32x32x64_f8f6f4 v[114:129], v[206:213], v[146:153], v[114:129]
	v_add_f32_e32 v182, v87, v182
	v_exp_f32_e32 v92, v92
	v_exp_f32_e32 v94, v94
	v_exp_f32_e32 v95, v95
	v_add_f32_e32 v182, v88, v182
	v_exp_f32_e32 v93, v93
	v_add_f32_e32 v182, v89, v182
	v_add_f32_e32 v182, v90, v182
	v_add_f32_e32 v182, v91, v182
	v_exp_f32_e32 v96, v96
	v_exp_f32_e32 v97, v97
	v_add_f32_e32 v182, v92, v182
	v_cvt_pk_fp8_f32 v130, v235, v236
	v_cvt_pk_fp8_f32 v134, v82, v83
	v_cvt_pk_fp8_f32 v131, v231, v232
	v_mfma_f32_32x32x64_f8f6f4 v[98:113], v[238:245], v[146:153], v[98:113]
	ds_read_b128 v[206:209], v200 offset:20480
	ds_read_b128 v[210:213], v201 offset:20480
	ds_read_b128 v[238:241], v200 offset:26624
	ds_read_b128 v[242:245], v201 offset:26624
	v_cvt_pk_fp8_f32 v135, v86, v87
	v_cvt_pk_fp8_f32 v132, v227, v228
	v_cvt_pk_fp8_f32 v136, v90, v91
	v_cvt_pk_fp8_f32 v133, v223, v224
	v_cvt_pk_fp8_f32 v137, v94, v95
	v_add_f32_e32 v182, v93, v182
	v_add_f32_e32 v182, v94, v182
	v_add_f32_e32 v182, v95, v182
	v_add_f32_e32 v182, v96, v182
	v_cvt_pk_fp8_f32 v130, v233, v234 op_sel:[0,0,1]
	v_cvt_pk_fp8_f32 v134, v84, v85 op_sel:[0,0,1]
	v_cvt_pk_fp8_f32 v131, v229, v230 op_sel:[0,0,1]
	v_cvt_pk_fp8_f32 v135, v88, v89 op_sel:[0,0,1]
	v_cvt_pk_fp8_f32 v132, v225, v226 op_sel:[0,0,1]
	s_waitcnt lgkmcnt(0)
	v_mfma_f32_32x32x64_f8f6f4 v[114:129], v[206:213], v[154:161], v[114:129]
	v_cvt_pk_fp8_f32 v136, v92, v93 op_sel:[0,0,1]
	v_cvt_pk_fp8_f32 v133, v221, v222 op_sel:[0,0,1]
	v_cvt_pk_fp8_f32 v137, v96, v97 op_sel:[0,0,1]
	v_add_f32_e32 v206, v97, v182
	v_mov_b32_e32 v207, v206
	s_nop 1
	v_permlane32_swap_b32_e32 v206, v207
	v_mfma_f32_32x32x64_f8f6f4 v[98:113], v[238:245], v[154:161], v[98:113]
	v_add_u32_e32 v194, v204, v203
	v_add_u32_e32 v193, v204, v202
	ds_read_b128 v[86:89], v194
	ds_read_b128 v[82:85], v193
	ds_read_b128 v[90:93], v193 offset:2048
	ds_read_b128 v[94:97], v194 offset:2048
	s_nop 4
	v_max_f32_e32 v182, v115, v115
	v_max_f32_e32 v183, v114, v114
	v_max_f32_e32 v182, v183, v182
	s_waitcnt lgkmcnt(0)
	v_mfma_f32_32x32x64_f8f6f4 v[2:17], v[130:137], v[82:89], v[2:17]
	v_max3_f32 v182, v182, v116, v117
	v_max3_f32 v182, v182, v118, v119
	v_max3_f32 v182, v182, v120, v121
	v_max3_f32 v182, v182, v122, v123
	v_max3_f32 v182, v182, v124, v125
	v_max3_f32 v182, v182, v126, v127
	v_max3_f32 v182, v182, v128, v129
	v_max3_f32 v182, v182, v98, v99
	v_mov_b32_e32 v208, 1.0
	v_mfma_f32_32x32x64_f8f6f4 v[50:65], v[130:137], v[90:97], v[50:65]
	ds_read_b128 v[82:85], v193 offset:4096
	ds_read_b128 v[90:93], v193 offset:6144
	ds_read_b128 v[86:89], v194 offset:4096
	ds_read_b128 v[94:97], v194 offset:6144
	s_waitcnt lgkmcnt(0)
	v_mfma_f32_32x32x64_f8f6f4 v[34:49], v[130:137], v[82:89], v[34:49]
	v_max3_f32 v82, v182, v100, v101
	v_max3_f32 v82, v82, v102, v103
	v_max3_f32 v82, v82, v104, v105
	v_max3_f32 v82, v82, v106, v107
	v_max3_f32 v82, v82, v108, v109
	v_max3_f32 v82, v82, v110, v111
	v_max3_f32 v82, v82, v112, v113
	v_mov_b32_e32 v83, v82
	s_nop 1
	v_permlane32_swap_b32_e32 v82, v83
	v_max_f32_e32 v83, v83, v83
	v_max_f32_e32 v82, v82, v82
	v_max_f32_e32 v82, v82, v83
	v_cmp_ge_f32_e32 vcc, s85, v82
	s_cmp_eq_u64 vcc, exec
	v_mfma_f32_32x32x64_f8f6f4 v[18:33], v[130:137], v[90:97], v[18:33]
	s_cbranch_scc0 .LBB0_931
	v_cmp_gt_f32_e32 vcc, 1.0, v208
	s_cbranch_vccz .LBB0_894

; __device__ __forceinline__ void finishSM(f32x16& p0, f32x16& p1, float alpha, float& l_reg, v8i& pa) {
; #pragma unroll
;   for (int r = 0; r < 16; ++r) p1[r] = __builtin_amdgcn_exp2f(p1[r]);
;   float ps = 0;
; #pragma unroll
;   for (int r = 0; r < 16; ++r) ps += p0[r];
; #pragma unroll
;   for (int r = 0; r < 16; ++r) ps += p1[r];
;   { auto rr = __builtin_amdgcn_permlane32_swap(__float_as_uint(ps), __float_as_uint(ps), false, false);
;     ps = __uint_as_float(rr[0]) + __uint_as_float(rr[1]); }
;   l_reg = l_reg * alpha + ps;
; #pragma unroll
;   for (int q = 0; q < 4; ++q) { int w0 = pa[q], w1 = pa[4 + q];
;     w0 = __builtin_amdgcn_cvt_pk_fp8_f32(p0[4 * q], p0[4 * q + 1], w0, false); w0 = __builtin_amdgcn_cvt_pk_fp8_f32(p0[4 * q + 2], p0[4 * q + 3], w0, true);
;     w1 = __builtin_amdgcn_cvt_pk_fp8_f32(p1[4 * q], p1[4 * q + 1], w1, false); w1 = __builtin_amdgcn_cvt_pk_fp8_f32(p1[4 * q + 2], p1[4 * q + 3], w1, true);
;     pa[q] = w0; pa[4 + q] = w1; }
; }
; __device__ __forceinline__ void qkt(f32x16& p0, f32x16& p1, const char* Ks, const v8i* qr, int r32, int hi, const f32x16& nm16) {
; #pragma unroll
;   for (int s = 0; s < 3; ++s) { const int c0 = 4 * s + 2 * hi;
;     const v8i a0 = __builtin_shufflevector(*reinterpret_cast<const v4i*>(Ks + k8_off(r32, c0)), *reinterpret_cast<const v4i*>(Ks + k8_off(r32, c0 + 1)), 0, 1, 2, 3, 4, 5, 6, 7);
;     const v8i a1 = __builtin_shufflevector(*reinterpret_cast<const v4i*>(Ks + 32 * DQK + k8_off(r32, c0)), *reinterpret_cast<const v4i*>(Ks + 32 * DQK + k8_off(r32, c0 + 1)), 0, 1, 2, 3, 4, 5, 6, 7);
;     p0 = __builtin_amdgcn_mfma_scale_f32_32x32x64_f8f6f4(a0, qr[s], s == 0 ? nm16 : p0, 0, 0, 0, 0, 0, 0);
;     p1 = __builtin_amdgcn_mfma_scale_f32_32x32x64_f8f6f4(a1, qr[s], s == 0 ? nm16 : p1, 0, 0, 0, 0, 0, 0); }
; }
; __device__ __forceinline__ void pv_d0(f32x16* o, const char* Vs, v8i pa, int r32, int hi) {
; #pragma unroll
;   for (int d0 = 0; d0 < 4; ++d0) { const int row = 32 * d0 + r32, x = (row >> 2) & 3;
;     const v8i vb = __builtin_shufflevector(*reinterpret_cast<const v4i*>(Vs + row * 64 + (((2 * hi) ^ x) << 4)), *reinterpret_cast<const v4i*>(Vs + row * 64 + (((2 * hi + 1) ^ x) << 4)), 0, 1, 2, 3, 4, 5, 6, 7);
;     o[d0] = __builtin_amdgcn_mfma_scale_f32_32x32x64_f8f6f4(pa, vb, o[d0], 0, 0, 0, 0, 0, 0); }
; }
.LBB0_894:
	s_waitcnt vmcnt(0)
	s_mov_b32 m0, s87
	s_barrier
	v_exp_f32_e32 v182, v114
	v_exp_f32_e32 v183, v115
	v_exp_f32_e32 v184, v116
	v_exp_f32_e32 v185, v117
	v_exp_f32_e32 v226, v118
	v_exp_f32_e32 v227, v119
	v_exp_f32_e32 v228, v120
	v_exp_f32_e32 v229, v121
	v_exp_f32_e32 v230, v122
	v_exp_f32_e32 v231, v123
	v_exp_f32_e32 v232, v124
	v_exp_f32_e32 v233, v125
	v_exp_f32_e32 v234, v126
	v_exp_f32_e32 v235, v127
	v_exp_f32_e32 v236, v128
	v_exp_f32_e32 v237, v129
	ds_read_b128 v[82:85], v196 offset:49152
	ds_read_b128 v[86:89], v197 offset:49152
	ds_read_b128 v[210:213], v196 offset:55296
	ds_read_b128 v[214:217], v197 offset:55296
	v_add_f32_e32 v209, 0, v182
	v_add_f32_e32 v209, v183, v209
	s_waitcnt lgkmcnt(0)
	v_mfma_f32_32x32x64_f8f6f4 v[114:129], v[82:89], v[138:145], v[66:81]
	v_add_f32_e32 v209, v184, v209
	v_add_f32_e32 v209, v185, v209
	v_add_f32_e32 v209, v226, v209
	v_add_f32_e32 v209, v227, v209
	v_add_f32_e32 v209, v228, v209
	v_add_f32_e32 v209, v229, v209
	v_add_f32_e32 v209, v230, v209
	v_add_f32_e32 v209, v231, v209
	v_add_f32_e32 v209, v232, v209
	v_add_f32_e32 v209, v233, v209
	v_exp_f32_e32 v98, v98
	v_add_f32_e32 v209, v234, v209
	v_exp_f32_e32 v99, v99
	v_add_f32_e32 v209, v235, v209
	v_exp_f32_e32 v100, v100
	v_mfma_f32_32x32x64_f8f6f4 v[82:97], v[210:217], v[138:145], v[66:81]
	v_lshl_add_u64 v[218:219], v[178:179], 0, s[30:31]
	global_load_lds_dwordx4 v[218:219], off
	s_and_b64 vcc, exec, s[4:5]
	s_cbranch_vccnz .LBB0_896
	v_lshl_add_u64 v[218:219], v[180:181], 0, s[30:31]
	s_add_i32 m0, s86, 0x4000
	s_nop 0
	global_load_lds_dwordx4 v[218:219], off
.LBB0_896:
	s_mov_b32 m0, s86
	v_lshl_add_u64 v[218:219], v[176:177], 0, s[34:35]
	global_load_lds_dwordx4 v[218:219], off
	ds_read_b128 v[210:213], v198 offset:49152
	ds_read_b128 v[214:217], v199 offset:49152
	ds_read_b128 v[218:221], v198 offset:55296
	ds_read_b128 v[222:225], v199 offset:55296
	v_add_f32_e32 v209, v236, v209
	v_exp_f32_e32 v101, v101
	v_add_f32_e32 v209, v237, v209
	v_exp_f32_e32 v102, v102
	v_add_f32_e32 v209, v98, v209
	v_exp_f32_e32 v103, v103
	v_add_f32_e32 v209, v99, v209
	v_exp_f32_e32 v104, v104
	v_add_f32_e32 v209, v100, v209
	v_exp_f32_e32 v105, v105
	v_add_f32_e32 v209, v101, v209
	v_exp_f32_e32 v106, v106
	v_add_f32_e32 v209, v102, v209
	v_exp_f32_e32 v107, v107
	s_waitcnt lgkmcnt(0)
	v_mfma_f32_32x32x64_f8f6f4 v[114:129], v[210:217], v[146:153], v[114:129]
	v_add_f32_e32 v209, v103, v209
	v_exp_f32_e32 v108, v108
	v_exp_f32_e32 v110, v110
	v_exp_f32_e32 v111, v111
	v_add_f32_e32 v209, v104, v209
	v_exp_f32_e32 v109, v109
	v_add_f32_e32 v209, v105, v209
	v_add_f32_e32 v209, v106, v209
	v_add_f32_e32 v209, v107, v209
	v_exp_f32_e32 v112, v112
	v_exp_f32_e32 v113, v113
	v_add_f32_e32 v209, v108, v209
	v_cvt_pk_fp8_f32 v130, v182, v183
	v_cvt_pk_fp8_f32 v134, v98, v99
	v_cvt_pk_fp8_f32 v131, v226, v227
	v_mfma_f32_32x32x64_f8f6f4 v[82:97], v[218:225], v[146:153], v[82:97]
	ds_read_b128 v[210:213], v200 offset:49152
	ds_read_b128 v[214:217], v201 offset:49152
	ds_read_b128 v[218:221], v200 offset:55296
	ds_read_b128 v[222:225], v201 offset:55296
	v_cvt_pk_fp8_f32 v135, v102, v103
	v_cvt_pk_fp8_f32 v132, v230, v231
	v_cvt_pk_fp8_f32 v136, v106, v107
	v_cvt_pk_fp8_f32 v133, v234, v235
	v_cvt_pk_fp8_f32 v137, v110, v111
	v_add_f32_e32 v209, v109, v209
	v_add_f32_e32 v209, v110, v209
	v_add_f32_e32 v209, v111, v209
	v_add_f32_e32 v209, v112, v209
	v_cvt_pk_fp8_f32 v130, v184, v185 op_sel:[0,0,1]
	v_cvt_pk_fp8_f32 v134, v100, v101 op_sel:[0,0,1]
	v_cvt_pk_fp8_f32 v131, v228, v229 op_sel:[0,0,1]
	v_cvt_pk_fp8_f32 v135, v104, v105 op_sel:[0,0,1]
	v_cvt_pk_fp8_f32 v132, v232, v233 op_sel:[0,0,1]
	s_waitcnt lgkmcnt(0)
	v_mfma_f32_32x32x64_f8f6f4 v[114:129], v[210:217], v[154:161], v[114:129]
	v_cvt_pk_fp8_f32 v136, v108, v109 op_sel:[0,0,1]
	v_cvt_pk_fp8_f32 v133, v236, v237 op_sel:[0,0,1]
	v_cvt_pk_fp8_f32 v137, v112, v113 op_sel:[0,0,1]
	v_add_f32_e32 v209, v113, v209
	v_mov_b32_e32 v210, v209
	s_nop 1
	v_permlane32_swap_b32_e32 v209, v210
	v_mfma_f32_32x32x64_f8f6f4 v[82:97], v[218:225], v[154:161], v[82:97]
	ds_read_b128 v[102:105], v194 offset:32768
	ds_read_b128 v[98:101], v193 offset:32768
	ds_read_b128 v[106:109], v193 offset:34816
	ds_read_b128 v[110:113], v194 offset:34816
	s_nop 6
	v_max_f32_e32 v182, v115, v115
	v_max_f32_e32 v183, v114, v114
	v_max_f32_e32 v182, v183, v182
	s_waitcnt lgkmcnt(0)
	v_mfma_f32_32x32x64_f8f6f4 v[2:17], v[130:137], v[98:105], v[2:17]
	v_max3_f32 v182, v182, v116, v117
	v_max3_f32 v182, v182, v118, v119
	v_max3_f32 v182, v182, v120, v121
	v_max3_f32 v182, v182, v122, v123
	v_max3_f32 v182, v182, v124, v125
	v_max3_f32 v182, v182, v126, v127
	v_max3_f32 v182, v182, v128, v129
	v_max3_f32 v182, v182, v82, v83
	v_mov_b32_e32 v211, 1.0
	v_mfma_f32_32x32x64_f8f6f4 v[50:65], v[130:137], v[106:113], v[50:65]
	ds_read_b128 v[98:101], v193 offset:36864
	ds_read_b128 v[106:109], v193 offset:38912
	ds_read_b128 v[102:105], v194 offset:36864
	ds_read_b128 v[110:113], v194 offset:38912
	s_waitcnt lgkmcnt(0)
	v_mfma_f32_32x32x64_f8f6f4 v[34:49], v[130:137], v[98:105], v[34:49]
	v_max3_f32 v98, v182, v84, v85
	v_max3_f32 v98, v98, v86, v87
	v_max3_f32 v98, v98, v88, v89
	v_max3_f32 v98, v98, v90, v91
	v_max3_f32 v98, v98, v92, v93
	v_max3_f32 v98, v98, v94, v95
	v_max3_f32 v98, v98, v96, v97
	v_mov_b32_e32 v99, v98
	s_nop 1
	v_permlane32_swap_b32_e32 v98, v99
	v_max_f32_e32 v99, v99, v99
	v_max_f32_e32 v98, v98, v98
	v_max_f32_e32 v98, v98, v99
	v_cmp_ge_f32_e32 vcc, s85, v98
	s_cmp_eq_u64 vcc, exec
	v_mfma_f32_32x32x64_f8f6f4 v[18:33], v[130:137], v[106:113], v[18:33]
	s_cbranch_scc0 .LBB0_932
	v_cmp_gt_f32_e32 vcc, 1.0, v211
	s_cbranch_vccz .LBB0_901

; __device__ __forceinline__ void finishSM(f32x16& p0, f32x16& p1, float alpha, float& l_reg, v8i& pa) {
; #pragma unroll
;   for (int r = 0; r < 16; ++r) p1[r] = __builtin_amdgcn_exp2f(p1[r]);
;   float ps = 0;
; #pragma unroll
;   for (int r = 0; r < 16; ++r) ps += p0[r];
; #pragma unroll
;   for (int r = 0; r < 16; ++r) ps += p1[r];
;   { auto rr = __builtin_amdgcn_permlane32_swap(__float_as_uint(ps), __float_as_uint(ps), false, false);
;     ps = __uint_as_float(rr[0]) + __uint_as_float(rr[1]); }
;   l_reg = l_reg * alpha + ps;
; #pragma unroll
;   for (int q = 0; q < 4; ++q) { int w0 = pa[q], w1 = pa[4 + q];
;     w0 = __builtin_amdgcn_cvt_pk_fp8_f32(p0[4 * q], p0[4 * q + 1], w0, false); w0 = __builtin_amdgcn_cvt_pk_fp8_f32(p0[4 * q + 2], p0[4 * q + 3], w0, true);
;     w1 = __builtin_amdgcn_cvt_pk_fp8_f32(p1[4 * q], p1[4 * q + 1], w1, false); w1 = __builtin_amdgcn_cvt_pk_fp8_f32(p1[4 * q + 2], p1[4 * q + 3], w1, true);
;     pa[q] = w0; pa[4 + q] = w1; }
; }
; __device__ __forceinline__ void qkt(f32x16& p0, f32x16& p1, const char* Ks, const v8i* qr, int r32, int hi, const f32x16& nm16) {
; #pragma unroll
;   for (int s = 0; s < 3; ++s) { const int c0 = 4 * s + 2 * hi;
;     const v8i a0 = __builtin_shufflevector(*reinterpret_cast<const v4i*>(Ks + k8_off(r32, c0)), *reinterpret_cast<const v4i*>(Ks + k8_off(r32, c0 + 1)), 0, 1, 2, 3, 4, 5, 6, 7);
;     const v8i a1 = __builtin_shufflevector(*reinterpret_cast<const v4i*>(Ks + 32 * DQK + k8_off(r32, c0)), *reinterpret_cast<const v4i*>(Ks + 32 * DQK + k8_off(r32, c0 + 1)), 0, 1, 2, 3, 4, 5, 6, 7);
;     p0 = __builtin_amdgcn_mfma_scale_f32_32x32x64_f8f6f4(a0, qr[s], s == 0 ? nm16 : p0, 0, 0, 0, 0, 0, 0);
;     p1 = __builtin_amdgcn_mfma_scale_f32_32x32x64_f8f6f4(a1, qr[s], s == 0 ? nm16 : p1, 0, 0, 0, 0, 0, 0); }
; }
; __device__ __forceinline__ void pv_d0(f32x16* o, const char* Vs, v8i pa, int r32, int hi) {
; #pragma unroll
;   for (int d0 = 0; d0 < 4; ++d0) { const int row = 32 * d0 + r32, x = (row >> 2) & 3;
;     const v8i vb = __builtin_shufflevector(*reinterpret_cast<const v4i*>(Vs + row * 64 + (((2 * hi) ^ x) << 4)), *reinterpret_cast<const v4i*>(Vs + row * 64 + (((2 * hi + 1) ^ x) << 4)), 0, 1, 2, 3, 4, 5, 6, 7);
;     o[d0] = __builtin_amdgcn_mfma_scale_f32_32x32x64_f8f6f4(pa, vb, o[d0], 0, 0, 0, 0, 0, 0); }
; }
.LBB0_901:
	s_waitcnt vmcnt(0)
	s_mov_b32 m0, s92
	s_barrier
	v_exp_f32_e32 v182, v114
	v_exp_f32_e32 v183, v115
	v_exp_f32_e32 v184, v116
	v_exp_f32_e32 v185, v117
	v_exp_f32_e32 v228, v118
	v_exp_f32_e32 v229, v119
	v_exp_f32_e32 v230, v120
	v_exp_f32_e32 v231, v121
	v_exp_f32_e32 v232, v122
	v_exp_f32_e32 v233, v123
	v_exp_f32_e32 v234, v124
	v_exp_f32_e32 v235, v125
	v_exp_f32_e32 v236, v126
	v_exp_f32_e32 v237, v127
	v_exp_f32_e32 v238, v128
	v_exp_f32_e32 v239, v129
	ds_read_b128 v[98:101], v196 offset:8192
	ds_read_b128 v[102:105], v197 offset:8192
	ds_read_b128 v[212:215], v196 offset:14336
	ds_read_b128 v[216:219], v197 offset:14336
	v_exp_f32_e32 v82, v82
	v_exp_f32_e32 v83, v83
	s_waitcnt lgkmcnt(0)
	v_mfma_f32_32x32x64_f8f6f4 v[114:129], v[98:105], v[138:145], v[66:81]
	v_exp_f32_e32 v84, v84
	v_exp_f32_e32 v85, v85
	v_exp_f32_e32 v86, v86
	v_exp_f32_e32 v87, v87
	v_exp_f32_e32 v88, v88
	v_exp_f32_e32 v89, v89
	v_exp_f32_e32 v90, v90
	v_exp_f32_e32 v91, v91
	v_exp_f32_e32 v92, v92
	v_exp_f32_e32 v94, v94
	v_exp_f32_e32 v95, v95
	v_exp_f32_e32 v93, v93
	v_exp_f32_e32 v96, v96
	v_exp_f32_e32 v97, v97
	v_cvt_pk_fp8_f32 v130, v182, v183
	v_mfma_f32_32x32x64_f8f6f4 v[98:113], v[212:219], v[138:145], v[66:81]
	v_lshl_add_u64 v[220:221], v[178:179], 0, s[36:37]
	global_load_lds_dwordx4 v[220:221], off
	s_and_b64 vcc, exec, s[4:5]
	s_cbranch_vccnz .LBB0_903
	v_lshl_add_u64 v[220:221], v[180:181], 0, s[36:37]
	s_add_i32 m0, s86, 0x7000
	s_nop 0
	global_load_lds_dwordx4 v[220:221], off
.LBB0_903:
	s_mov_b32 m0, s88
	v_lshl_add_u64 v[220:221], v[176:177], 0, s[38:39]
	global_load_lds_dwordx4 v[220:221], off
	ds_read_b128 v[212:215], v198 offset:8192
	ds_read_b128 v[216:219], v199 offset:8192
	ds_read_b128 v[220:223], v198 offset:14336
	ds_read_b128 v[224:227], v199 offset:14336
	v_cvt_pk_fp8_f32 v134, v82, v83
	v_cvt_pk_fp8_f32 v131, v228, v229
	v_cvt_pk_fp8_f32 v135, v86, v87
	v_cvt_pk_fp8_f32 v132, v232, v233
	v_cvt_pk_fp8_f32 v136, v90, v91
	v_cvt_pk_fp8_f32 v133, v236, v237
	v_cvt_pk_fp8_f32 v137, v94, v95
	v_cvt_pk_fp8_f32 v130, v184, v185 op_sel:[0,0,1]
	v_cvt_pk_fp8_f32 v134, v84, v85 op_sel:[0,0,1]
	v_cvt_pk_fp8_f32 v131, v230, v231 op_sel:[0,0,1]
	v_cvt_pk_fp8_f32 v135, v88, v89 op_sel:[0,0,1]
	v_cvt_pk_fp8_f32 v132, v234, v235 op_sel:[0,0,1]
	v_cvt_pk_fp8_f32 v136, v92, v93 op_sel:[0,0,1]
	v_cvt_pk_fp8_f32 v133, v238, v239 op_sel:[0,0,1]
	s_waitcnt lgkmcnt(0)
	v_mfma_f32_32x32x64_f8f6f4 v[114:129], v[212:219], v[146:153], v[114:129]
	v_cvt_pk_fp8_f32 v137, v96, v97 op_sel:[0,0,1]
	v_mfma_f32_32x32x64_f8f6f4 v[98:113], v[220:227], v[146:153], v[98:113]
	ds_read_b128 v[212:215], v200 offset:8192
	ds_read_b128 v[216:219], v201 offset:8192
	ds_read_b128 v[220:223], v200 offset:14336
	ds_read_b128 v[224:227], v201 offset:14336
	s_waitcnt lgkmcnt(0)
	v_mfma_f32_32x32x64_f8f6f4 v[114:129], v[212:219], v[154:161], v[114:129]
	v_add_f32_e32 v212, 0, v182
	v_add_f32_e32 v212, v183, v212
	v_add_f32_e32 v212, v184, v212
	v_add_f32_e32 v212, v185, v212
	v_add_f32_e32 v212, v228, v212
	v_add_f32_e32 v212, v229, v212
	v_add_f32_e32 v212, v230, v212
	v_add_f32_e32 v212, v231, v212
	v_add_f32_e32 v212, v232, v212
	v_add_f32_e32 v212, v233, v212
	v_add_f32_e32 v212, v234, v212
	v_add_f32_e32 v212, v235, v212
	v_add_f32_e32 v212, v236, v212
	v_add_f32_e32 v212, v237, v212
	v_add_f32_e32 v212, v238, v212
	v_add_f32_e32 v212, v239, v212
	v_add_f32_e32 v212, v82, v212
	v_add_f32_e32 v212, v83, v212
	v_mfma_f32_32x32x64_f8f6f4 v[98:113], v[220:227], v[154:161], v[98:113]
	v_add_f32_e32 v212, v84, v212
	v_add_f32_e32 v212, v85, v212
	v_add_f32_e32 v212, v86, v212
	v_add_f32_e32 v212, v87, v212
	v_add_f32_e32 v212, v88, v212
	v_add_f32_e32 v212, v89, v212
	v_add_f32_e32 v212, v90, v212
	v_add_f32_e32 v212, v91, v212
	v_add_f32_e32 v212, v92, v212
	v_add_f32_e32 v212, v93, v212
	v_add_f32_e32 v212, v94, v212
	v_add_f32_e32 v212, v95, v212
	v_add_f32_e32 v212, v96, v212
	v_add_f32_e32 v212, v97, v212
	v_mov_b32_e32 v213, v212
	s_nop 1
	v_permlane32_swap_b32_e32 v212, v213
	ds_read_b128 v[86:89], v194 offset:40960
	ds_read_b128 v[82:85], v193 offset:40960
	ds_read_b128 v[90:93], v193 offset:43008
	ds_read_b128 v[94:97], v194 offset:43008
	v_max_f32_e32 v182, v115, v115
	v_max_f32_e32 v183, v114, v114
	v_max_f32_e32 v182, v183, v182
	s_waitcnt lgkmcnt(0)
	v_mfma_f32_32x32x64_f8f6f4 v[2:17], v[130:137], v[82:89], v[2:17]
	v_max3_f32 v182, v182, v116, v117
	v_max3_f32 v182, v182, v118, v119
	v_max3_f32 v182, v182, v120, v121
	v_max3_f32 v182, v182, v122, v123
	v_max3_f32 v182, v182, v124, v125
	v_max3_f32 v182, v182, v126, v127
	v_max3_f32 v182, v182, v128, v129
	v_max3_f32 v182, v182, v98, v99
	v_mov_b32_e32 v214, 1.0
	v_mfma_f32_32x32x64_f8f6f4 v[50:65], v[130:137], v[90:97], v[50:65]
	ds_read_b128 v[82:85], v193 offset:45056
	ds_read_b128 v[90:93], v193 offset:47104
	ds_read_b128 v[86:89], v194 offset:45056
	ds_read_b128 v[94:97], v194 offset:47104
	s_waitcnt lgkmcnt(0)
	v_mfma_f32_32x32x64_f8f6f4 v[34:49], v[130:137], v[82:89], v[34:49]
	v_max3_f32 v82, v182, v100, v101
	v_max3_f32 v82, v82, v102, v103
	v_max3_f32 v82, v82, v104, v105
	v_max3_f32 v82, v82, v106, v107
	v_max3_f32 v82, v82, v108, v109
	v_max3_f32 v82, v82, v110, v111
	v_max3_f32 v82, v82, v112, v113
	v_mov_b32_e32 v83, v82
	s_nop 1
	v_permlane32_swap_b32_e32 v82, v83
	v_max_f32_e32 v83, v83, v83
	v_max_f32_e32 v82, v82, v82
	v_max_f32_e32 v82, v82, v83
	v_cmp_ge_f32_e32 vcc, s85, v82
	s_cmp_eq_u64 vcc, exec
	v_mfma_f32_32x32x64_f8f6f4 v[18:33], v[130:137], v[90:97], v[18:33]
	s_cbranch_scc0 .LBB0_933
	v_cmp_gt_f32_e32 vcc, 1.0, v214
	s_cbranch_vccz .LBB0_908

; __device__ __forceinline__ void finishSM(f32x16& p0, f32x16& p1, float alpha, float& l_reg, v8i& pa) {
; #pragma unroll
;   for (int r = 0; r < 16; ++r) p1[r] = __builtin_amdgcn_exp2f(p1[r]);
;   float ps = 0;
; #pragma unroll
;   for (int r = 0; r < 16; ++r) ps += p0[r];
; #pragma unroll
;   for (int r = 0; r < 16; ++r) ps += p1[r];
;   { auto rr = __builtin_amdgcn_permlane32_swap(__float_as_uint(ps), __float_as_uint(ps), false, false);
;     ps = __uint_as_float(rr[0]) + __uint_as_float(rr[1]); }
;   l_reg = l_reg * alpha + ps;
; #pragma unroll
;   for (int q = 0; q < 4; ++q) { int w0 = pa[q], w1 = pa[4 + q];
;     w0 = __builtin_amdgcn_cvt_pk_fp8_f32(p0[4 * q], p0[4 * q + 1], w0, false); w0 = __builtin_amdgcn_cvt_pk_fp8_f32(p0[4 * q + 2], p0[4 * q + 3], w0, true);
;     w1 = __builtin_amdgcn_cvt_pk_fp8_f32(p1[4 * q], p1[4 * q + 1], w1, false); w1 = __builtin_amdgcn_cvt_pk_fp8_f32(p1[4 * q + 2], p1[4 * q + 3], w1, true);
;     pa[q] = w0; pa[4 + q] = w1; }
; }
; __device__ __forceinline__ void qkt(f32x16& p0, f32x16& p1, const char* Ks, const v8i* qr, int r32, int hi, const f32x16& nm16) {
; #pragma unroll
;   for (int s = 0; s < 3; ++s) { const int c0 = 4 * s + 2 * hi;
;     const v8i a0 = __builtin_shufflevector(*reinterpret_cast<const v4i*>(Ks + k8_off(r32, c0)), *reinterpret_cast<const v4i*>(Ks + k8_off(r32, c0 + 1)), 0, 1, 2, 3, 4, 5, 6, 7);
;     const v8i a1 = __builtin_shufflevector(*reinterpret_cast<const v4i*>(Ks + 32 * DQK + k8_off(r32, c0)), *reinterpret_cast<const v4i*>(Ks + 32 * DQK + k8_off(r32, c0 + 1)), 0, 1, 2, 3, 4, 5, 6, 7);
;     p0 = __builtin_amdgcn_mfma_scale_f32_32x32x64_f8f6f4(a0, qr[s], s == 0 ? nm16 : p0, 0, 0, 0, 0, 0, 0);
;     p1 = __builtin_amdgcn_mfma_scale_f32_32x32x64_f8f6f4(a1, qr[s], s == 0 ? nm16 : p1, 0, 0, 0, 0, 0, 0); }
; }
; __device__ __forceinline__ void pv_d0(f32x16* o, const char* Vs, v8i pa, int r32, int hi) {
; #pragma unroll
;   for (int d0 = 0; d0 < 4; ++d0) { const int row = 32 * d0 + r32, x = (row >> 2) & 3;
;     const v8i vb = __builtin_shufflevector(*reinterpret_cast<const v4i*>(Vs + row * 64 + (((2 * hi) ^ x) << 4)), *reinterpret_cast<const v4i*>(Vs + row * 64 + (((2 * hi + 1) ^ x) << 4)), 0, 1, 2, 3, 4, 5, 6, 7);
;     o[d0] = __builtin_amdgcn_mfma_scale_f32_32x32x64_f8f6f4(pa, vb, o[d0], 0, 0, 0, 0, 0, 0); }
; }
.LBB0_908:
	s_waitcnt vmcnt(0)
	s_mov_b32 m0, s90
	s_barrier
	v_exp_f32_e32 v182, v114
	v_exp_f32_e32 v183, v115
	v_exp_f32_e32 v184, v116
	v_exp_f32_e32 v185, v117
	v_exp_f32_e32 v232, v118
	v_exp_f32_e32 v233, v119
	v_exp_f32_e32 v234, v120
	v_exp_f32_e32 v235, v121
	v_exp_f32_e32 v236, v122
	v_exp_f32_e32 v237, v123
	v_exp_f32_e32 v238, v124
	v_exp_f32_e32 v239, v125
	v_exp_f32_e32 v240, v126
	v_exp_f32_e32 v241, v127
	v_exp_f32_e32 v242, v128
	v_exp_f32_e32 v243, v129
	ds_read_b128 v[82:85], v196 offset:20480
	ds_read_b128 v[86:89], v197 offset:20480
	ds_read_b128 v[216:219], v196 offset:26624
	ds_read_b128 v[220:223], v197 offset:26624
	v_add_f32_e32 v215, 0, v182
	v_add_f32_e32 v215, v183, v215
	s_waitcnt lgkmcnt(0)
	v_mfma_f32_32x32x64_f8f6f4 v[114:129], v[82:89], v[138:145], v[66:81]
	v_add_f32_e32 v215, v184, v215
	v_add_f32_e32 v215, v185, v215
	v_add_f32_e32 v215, v232, v215
	v_add_f32_e32 v215, v233, v215
	v_add_f32_e32 v215, v234, v215
	v_add_f32_e32 v215, v235, v215
	v_add_f32_e32 v215, v236, v215
	v_add_f32_e32 v215, v237, v215
	v_add_f32_e32 v215, v238, v215
	v_add_f32_e32 v215, v239, v215
	v_exp_f32_e32 v98, v98
	v_add_f32_e32 v215, v240, v215
	v_exp_f32_e32 v99, v99
	v_add_f32_e32 v215, v241, v215
	v_exp_f32_e32 v100, v100
	v_mfma_f32_32x32x64_f8f6f4 v[82:97], v[216:223], v[138:145], v[66:81]
	v_lshl_add_u64 v[224:225], v[178:179], 0, s[40:41]
	global_load_lds_dwordx4 v[224:225], off
	s_and_b64 vcc, exec, s[4:5]
	s_cbranch_vccnz .LBB0_910
	v_lshl_add_u64 v[224:225], v[180:181], 0, s[40:41]
	s_mov_b32 m0, s91
	s_nop 0
	global_load_lds_dwordx4 v[224:225], off
.LBB0_910:
	s_mov_b32 m0, s89
	v_lshl_add_u64 v[224:225], v[176:177], 0, s[42:43]
	global_load_lds_dwordx4 v[224:225], off
	ds_read_b128 v[216:219], v198 offset:20480
	ds_read_b128 v[220:223], v199 offset:20480
	ds_read_b128 v[224:227], v198 offset:26624
	ds_read_b128 v[228:231], v199 offset:26624
	v_add_f32_e32 v215, v242, v215
	v_exp_f32_e32 v101, v101
	v_add_f32_e32 v215, v243, v215
	v_exp_f32_e32 v102, v102
	v_add_f32_e32 v215, v98, v215
	v_exp_f32_e32 v103, v103
	v_add_f32_e32 v215, v99, v215
	v_exp_f32_e32 v104, v104
	v_add_f32_e32 v215, v100, v215
	v_exp_f32_e32 v105, v105
	v_add_f32_e32 v215, v101, v215
	v_exp_f32_e32 v106, v106
	v_add_f32_e32 v215, v102, v215
	v_exp_f32_e32 v107, v107
	s_waitcnt lgkmcnt(0)
	v_mfma_f32_32x32x64_f8f6f4 v[114:129], v[216:223], v[146:153], v[114:129]
	v_add_f32_e32 v215, v103, v215
	v_exp_f32_e32 v108, v108
	v_exp_f32_e32 v110, v110
	v_exp_f32_e32 v111, v111
	v_add_f32_e32 v215, v104, v215
	v_exp_f32_e32 v109, v109
	v_add_f32_e32 v215, v105, v215
	v_add_f32_e32 v215, v106, v215
	v_add_f32_e32 v215, v107, v215
	v_exp_f32_e32 v112, v112
	v_exp_f32_e32 v113, v113
	v_add_f32_e32 v215, v108, v215
	v_cvt_pk_fp8_f32 v130, v182, v183
	v_cvt_pk_fp8_f32 v134, v98, v99
	v_cvt_pk_fp8_f32 v131, v232, v233
	v_mfma_f32_32x32x64_f8f6f4 v[82:97], v[224:231], v[146:153], v[82:97]
	ds_read_b128 v[216:219], v200 offset:20480
	ds_read_b128 v[220:223], v201 offset:20480
	ds_read_b128 v[224:227], v200 offset:26624
	ds_read_b128 v[228:231], v201 offset:26624
	v_cvt_pk_fp8_f32 v135, v102, v103
	v_cvt_pk_fp8_f32 v132, v236, v237
	v_cvt_pk_fp8_f32 v136, v106, v107
	v_cvt_pk_fp8_f32 v133, v240, v241
	v_cvt_pk_fp8_f32 v137, v110, v111
	v_add_f32_e32 v215, v109, v215
	v_add_f32_e32 v215, v110, v215
	v_add_f32_e32 v215, v111, v215
	v_add_f32_e32 v215, v112, v215
	v_cvt_pk_fp8_f32 v130, v184, v185 op_sel:[0,0,1]
	v_cvt_pk_fp8_f32 v134, v100, v101 op_sel:[0,0,1]
	v_cvt_pk_fp8_f32 v131, v234, v235 op_sel:[0,0,1]
	v_cvt_pk_fp8_f32 v135, v104, v105 op_sel:[0,0,1]
	v_cvt_pk_fp8_f32 v132, v238, v239 op_sel:[0,0,1]
	s_waitcnt lgkmcnt(0)
	v_mfma_f32_32x32x64_f8f6f4 v[114:129], v[216:223], v[154:161], v[114:129]
	v_cvt_pk_fp8_f32 v136, v108, v109 op_sel:[0,0,1]
	v_cvt_pk_fp8_f32 v133, v242, v243 op_sel:[0,0,1]
	v_cvt_pk_fp8_f32 v137, v112, v113 op_sel:[0,0,1]
	v_add_f32_e32 v215, v113, v215
	v_mov_b32_e32 v216, v215
	s_nop 1
	v_permlane32_swap_b32_e32 v215, v216
	v_mfma_f32_32x32x64_f8f6f4 v[82:97], v[224:231], v[154:161], v[82:97]
	ds_read_b128 v[102:105], v194
	ds_read_b128 v[98:101], v193
	ds_read_b128 v[106:109], v193 offset:2048
	ds_read_b128 v[110:113], v194 offset:2048
	s_nop 6
	v_max_f32_e32 v182, v115, v115
	v_max_f32_e32 v183, v114, v114
	v_max_f32_e32 v182, v183, v182
	s_waitcnt lgkmcnt(0)
	v_mfma_f32_32x32x64_f8f6f4 v[2:17], v[130:137], v[98:105], v[2:17]
	v_max3_f32 v182, v182, v116, v117
	v_max3_f32 v182, v182, v118, v119
	v_max3_f32 v182, v182, v120, v121
	v_max3_f32 v182, v182, v122, v123
	v_max3_f32 v182, v182, v124, v125
	v_max3_f32 v182, v182, v126, v127
	v_max3_f32 v182, v182, v128, v129
	v_max3_f32 v182, v182, v82, v83
	v_mov_b32_e32 v217, 1.0
	v_mfma_f32_32x32x64_f8f6f4 v[50:65], v[130:137], v[106:113], v[50:65]
	ds_read_b128 v[98:101], v193 offset:4096
	ds_read_b128 v[106:109], v193 offset:6144
	ds_read_b128 v[102:105], v194 offset:4096
	ds_read_b128 v[110:113], v194 offset:6144
	s_waitcnt lgkmcnt(0)
	v_mfma_f32_32x32x64_f8f6f4 v[34:49], v[130:137], v[98:105], v[34:49]
	v_max3_f32 v98, v182, v84, v85
	v_max3_f32 v98, v98, v86, v87
	v_max3_f32 v98, v98, v88, v89
	v_max3_f32 v98, v98, v90, v91
	v_max3_f32 v98, v98, v92, v93
	v_max3_f32 v98, v98, v94, v95
	v_max3_f32 v98, v98, v96, v97
	v_mov_b32_e32 v99, v98
	s_nop 1
	v_permlane32_swap_b32_e32 v98, v99
	v_max_f32_e32 v99, v99, v99
	v_max_f32_e32 v98, v98, v98
	v_max_f32_e32 v98, v98, v99
	v_cmp_ge_f32_e32 vcc, s85, v98
	s_cmp_eq_u64 vcc, exec
	v_mfma_f32_32x32x64_f8f6f4 v[18:33], v[130:137], v[106:113], v[18:33]
	s_cbranch_scc0 .LBB0_934
	v_cmp_gt_f32_e32 vcc, 1.0, v217
	s_cbranch_vccz .LBB0_915

; __device__ __forceinline__ void finishSM(f32x16& p0, f32x16& p1, float alpha, float& l_reg, v8i& pa) {
; #pragma unroll
;   for (int r = 0; r < 16; ++r) p1[r] = __builtin_amdgcn_exp2f(p1[r]);
;   float ps = 0;
; #pragma unroll
;   for (int r = 0; r < 16; ++r) ps += p0[r];
; #pragma unroll
;   for (int r = 0; r < 16; ++r) ps += p1[r];
;   { auto rr = __builtin_amdgcn_permlane32_swap(__float_as_uint(ps), __float_as_uint(ps), false, false);
;     ps = __uint_as_float(rr[0]) + __uint_as_float(rr[1]); }
;   l_reg = l_reg * alpha + ps;
; #pragma unroll
;   for (int q = 0; q < 4; ++q) { int w0 = pa[q], w1 = pa[4 + q];
;     w0 = __builtin_amdgcn_cvt_pk_fp8_f32(p0[4 * q], p0[4 * q + 1], w0, false); w0 = __builtin_amdgcn_cvt_pk_fp8_f32(p0[4 * q + 2], p0[4 * q + 3], w0, true);
;     w1 = __builtin_amdgcn_cvt_pk_fp8_f32(p1[4 * q], p1[4 * q + 1], w1, false); w1 = __builtin_amdgcn_cvt_pk_fp8_f32(p1[4 * q + 2], p1[4 * q + 3], w1, true);
;     pa[q] = w0; pa[4 + q] = w1; }
; }
; __device__ __forceinline__ void qkt(f32x16& p0, f32x16& p1, const char* Ks, const v8i* qr, int r32, int hi, const f32x16& nm16) {
; #pragma unroll
;   for (int s = 0; s < 3; ++s) { const int c0 = 4 * s + 2 * hi;
;     const v8i a0 = __builtin_shufflevector(*reinterpret_cast<const v4i*>(Ks + k8_off(r32, c0)), *reinterpret_cast<const v4i*>(Ks + k8_off(r32, c0 + 1)), 0, 1, 2, 3, 4, 5, 6, 7);
;     const v8i a1 = __builtin_shufflevector(*reinterpret_cast<const v4i*>(Ks + 32 * DQK + k8_off(r32, c0)), *reinterpret_cast<const v4i*>(Ks + 32 * DQK + k8_off(r32, c0 + 1)), 0, 1, 2, 3, 4, 5, 6, 7);
;     p0 = __builtin_amdgcn_mfma_scale_f32_32x32x64_f8f6f4(a0, qr[s], s == 0 ? nm16 : p0, 0, 0, 0, 0, 0, 0);
;     p1 = __builtin_amdgcn_mfma_scale_f32_32x32x64_f8f6f4(a1, qr[s], s == 0 ? nm16 : p1, 0, 0, 0, 0, 0, 0); }
; }
; __device__ __forceinline__ void pv_d0(f32x16* o, const char* Vs, v8i pa, int r32, int hi) {
; #pragma unroll
;   for (int d0 = 0; d0 < 4; ++d0) { const int row = 32 * d0 + r32, x = (row >> 2) & 3;
;     const v8i vb = __builtin_shufflevector(*reinterpret_cast<const v4i*>(Vs + row * 64 + (((2 * hi) ^ x) << 4)), *reinterpret_cast<const v4i*>(Vs + row * 64 + (((2 * hi + 1) ^ x) << 4)), 0, 1, 2, 3, 4, 5, 6, 7);
;     o[d0] = __builtin_amdgcn_mfma_scale_f32_32x32x64_f8f6f4(pa, vb, o[d0], 0, 0, 0, 0, 0, 0); }
; }
.LBB0_915:
	s_waitcnt vmcnt(0)
	s_mov_b32 m0, s87
	s_barrier
	v_exp_f32_e32 v182, v114
	v_exp_f32_e32 v183, v115
	v_exp_f32_e32 v184, v116
	v_exp_f32_e32 v185, v117
	v_exp_f32_e32 v234, v118
	v_exp_f32_e32 v235, v119
	v_exp_f32_e32 v236, v120
	v_exp_f32_e32 v237, v121
	v_exp_f32_e32 v238, v122
	v_exp_f32_e32 v239, v123
	v_exp_f32_e32 v240, v124
	v_exp_f32_e32 v241, v125
	v_exp_f32_e32 v242, v126
	v_exp_f32_e32 v243, v127
	v_exp_f32_e32 v244, v128
	v_exp_f32_e32 v245, v129
	ds_read_b128 v[98:101], v196 offset:49152
	ds_read_b128 v[102:105], v197 offset:49152
	ds_read_b128 v[218:221], v196 offset:55296
	ds_read_b128 v[222:225], v197 offset:55296
	v_exp_f32_e32 v82, v82
	v_exp_f32_e32 v83, v83
	s_waitcnt lgkmcnt(0)
	v_mfma_f32_32x32x64_f8f6f4 v[114:129], v[98:105], v[138:145], v[66:81]
	v_exp_f32_e32 v84, v84
	v_exp_f32_e32 v85, v85
	v_exp_f32_e32 v86, v86
	v_exp_f32_e32 v87, v87
	v_exp_f32_e32 v88, v88
	v_exp_f32_e32 v89, v89
	v_exp_f32_e32 v90, v90
	v_exp_f32_e32 v91, v91
	v_exp_f32_e32 v92, v92
	v_exp_f32_e32 v94, v94
	v_exp_f32_e32 v95, v95
	v_exp_f32_e32 v93, v93
	v_exp_f32_e32 v96, v96
	v_exp_f32_e32 v97, v97
	v_cvt_pk_fp8_f32 v130, v182, v183
	v_mfma_f32_32x32x64_f8f6f4 v[98:113], v[218:225], v[138:145], v[66:81]
	v_lshl_add_u64 v[226:227], v[178:179], 0, s[44:45]
	global_load_lds_dwordx4 v[226:227], off
	s_and_b64 vcc, exec, s[4:5]
	s_cbranch_vccnz .LBB0_917
	v_lshl_add_u64 v[226:227], v[180:181], 0, s[44:45]
	s_add_i32 m0, s86, 0x4000
	s_nop 0
	global_load_lds_dwordx4 v[226:227], off
.LBB0_917:
	s_mov_b32 m0, s86
	v_lshl_add_u64 v[226:227], v[176:177], 0, s[46:47]
	global_load_lds_dwordx4 v[226:227], off
	ds_read_b128 v[218:221], v198 offset:49152
	ds_read_b128 v[222:225], v199 offset:49152
	ds_read_b128 v[226:229], v198 offset:55296
	ds_read_b128 v[230:233], v199 offset:55296
	v_cvt_pk_fp8_f32 v134, v82, v83
	v_cvt_pk_fp8_f32 v131, v234, v235
	v_cvt_pk_fp8_f32 v135, v86, v87
	v_cvt_pk_fp8_f32 v132, v238, v239
	v_cvt_pk_fp8_f32 v136, v90, v91
	v_cvt_pk_fp8_f32 v133, v242, v243
	v_cvt_pk_fp8_f32 v137, v94, v95
	v_cvt_pk_fp8_f32 v130, v184, v185 op_sel:[0,0,1]
	v_cvt_pk_fp8_f32 v134, v84, v85 op_sel:[0,0,1]
	v_cvt_pk_fp8_f32 v131, v236, v237 op_sel:[0,0,1]
	v_cvt_pk_fp8_f32 v135, v88, v89 op_sel:[0,0,1]
	v_cvt_pk_fp8_f32 v132, v240, v241 op_sel:[0,0,1]
	v_cvt_pk_fp8_f32 v136, v92, v93 op_sel:[0,0,1]
	v_cvt_pk_fp8_f32 v133, v244, v245 op_sel:[0,0,1]
	s_waitcnt lgkmcnt(0)
	v_mfma_f32_32x32x64_f8f6f4 v[114:129], v[218:225], v[146:153], v[114:129]
	v_cvt_pk_fp8_f32 v137, v96, v97 op_sel:[0,0,1]
	v_mfma_f32_32x32x64_f8f6f4 v[98:113], v[226:233], v[146:153], v[98:113]
	ds_read_b128 v[218:221], v200 offset:49152
	ds_read_b128 v[222:225], v201 offset:49152
	ds_read_b128 v[226:229], v200 offset:55296
	ds_read_b128 v[230:233], v201 offset:55296
	s_waitcnt lgkmcnt(0)
	v_mfma_f32_32x32x64_f8f6f4 v[114:129], v[218:225], v[154:161], v[114:129]
	v_add_f32_e32 v218, 0, v182
	v_add_f32_e32 v218, v183, v218
	v_add_f32_e32 v218, v184, v218
	v_add_f32_e32 v218, v185, v218
	v_add_f32_e32 v218, v234, v218
	v_add_f32_e32 v218, v235, v218
	v_add_f32_e32 v218, v236, v218
	v_add_f32_e32 v218, v237, v218
	v_add_f32_e32 v218, v238, v218
	v_add_f32_e32 v218, v239, v218
	v_add_f32_e32 v218, v240, v218
	v_add_f32_e32 v218, v241, v218
	v_add_f32_e32 v218, v242, v218
	v_add_f32_e32 v218, v243, v218
	v_add_f32_e32 v218, v244, v218
	v_add_f32_e32 v218, v245, v218
	v_add_f32_e32 v218, v82, v218
	v_add_f32_e32 v218, v83, v218
	v_mfma_f32_32x32x64_f8f6f4 v[98:113], v[226:233], v[154:161], v[98:113]
	v_add_f32_e32 v218, v84, v218
	v_add_f32_e32 v218, v85, v218
	v_add_f32_e32 v218, v86, v218
	v_add_f32_e32 v218, v87, v218
	v_add_f32_e32 v218, v88, v218
	v_add_f32_e32 v218, v89, v218
	v_add_f32_e32 v218, v90, v218
	v_add_f32_e32 v218, v91, v218
	v_add_f32_e32 v218, v92, v218
	v_add_f32_e32 v218, v93, v218
	v_add_f32_e32 v218, v94, v218
	v_add_f32_e32 v218, v95, v218
	v_add_f32_e32 v218, v96, v218
	v_add_f32_e32 v218, v97, v218
	v_mov_b32_e32 v219, v218
	s_nop 1
	v_permlane32_swap_b32_e32 v218, v219
	ds_read_b128 v[86:89], v194 offset:32768
	ds_read_b128 v[82:85], v193 offset:32768
	ds_read_b128 v[90:93], v193 offset:34816
	ds_read_b128 v[94:97], v194 offset:34816
	v_max_f32_e32 v182, v115, v115
	v_max_f32_e32 v183, v114, v114
	v_max_f32_e32 v182, v183, v182
	s_waitcnt lgkmcnt(0)
	v_mfma_f32_32x32x64_f8f6f4 v[2:17], v[130:137], v[82:89], v[2:17]
	v_max3_f32 v182, v182, v116, v117
	v_max3_f32 v182, v182, v118, v119
	v_max3_f32 v182, v182, v120, v121
	v_max3_f32 v182, v182, v122, v123
	v_max3_f32 v182, v182, v124, v125
	v_max3_f32 v182, v182, v126, v127
	v_max3_f32 v182, v182, v128, v129
	v_max3_f32 v182, v182, v98, v99
	v_mov_b32_e32 v220, 1.0
	v_mfma_f32_32x32x64_f8f6f4 v[50:65], v[130:137], v[90:97], v[50:65]
	ds_read_b128 v[82:85], v193 offset:36864
	ds_read_b128 v[90:93], v193 offset:38912
	ds_read_b128 v[86:89], v194 offset:36864
	ds_read_b128 v[94:97], v194 offset:38912
	s_waitcnt lgkmcnt(0)
	v_mfma_f32_32x32x64_f8f6f4 v[34:49], v[130:137], v[82:89], v[34:49]
	v_max3_f32 v82, v182, v100, v101
	v_max3_f32 v82, v82, v102, v103
	v_max3_f32 v82, v82, v104, v105
	v_max3_f32 v82, v82, v106, v107
	v_max3_f32 v82, v82, v108, v109
	v_max3_f32 v82, v82, v110, v111
	v_max3_f32 v82, v82, v112, v113
	v_mov_b32_e32 v83, v82
	s_nop 1
	v_permlane32_swap_b32_e32 v82, v83
	v_max_f32_e32 v83, v83, v83
	v_max_f32_e32 v82, v82, v82
	v_max_f32_e32 v82, v82, v83
	v_cmp_ge_f32_e32 vcc, s85, v82
	s_cmp_eq_u64 vcc, exec
	v_mfma_f32_32x32x64_f8f6f4 v[18:33], v[130:137], v[90:97], v[18:33]
	s_cbranch_scc0 .LBB0_935
	v_cmp_gt_f32_e32 vcc, 1.0, v220
	s_cbranch_vccz .LBB0_922
